# attention PV: block-3 transposed V reads hoisted into block-2 MFMA shadow; compiler pad s_nop before PV MFMAs removed
# baseline (speedup 1.0000x reference)
; #define AT_SBAR() __builtin_amdgcn_sched_barrier(0)
; template <int OFF> DI s16x4 tr_read(int vb) { s16x4 r; asm volatile("ds_read_b64_tr_b16 %0, %1 offset:%2" : "=&v"(r) : "v"(vb), "i"(OFF) : "memory"); return r; }
; template <int D0> DI void pv_one(f32x16& od, int vb, bf16x8 pa0, bf16x8 pa1, bf16x8 pa2, bf16x8 pa3) {
;     const s16x4 l0 = tr_read<v_rd_off(D0, 0, 0)>(vb), h0 = tr_read<v_rd_off(D0, 0, 1)>(vb), l1 = tr_read<v_rd_off(D0, 1, 0)>(vb), h1 = tr_read<v_rd_off(D0, 1, 1)>(vb);
;     const s16x4 l2 = tr_read<v_rd_off(D0, 2, 0)>(vb), h2 = tr_read<v_rd_off(D0, 2, 1)>(vb), l3 = tr_read<v_rd_off(D0, 3, 0)>(vb), h3 = tr_read<v_rd_off(D0, 3, 1)>(vb);
;     asm volatile("s_waitcnt lgkmcnt(0)" ::: "memory"); AT_SBAR();
;     ...
;     od = __builtin_amdgcn_mfma_f32_32x32x16_bf16(AT_PK(l0, h0), pa0, od, 0, 0, 0);
;     od = __builtin_amdgcn_mfma_f32_32x32x16_bf16(AT_PK(l1, h1), pa1, od, 0, 0, 0);
;     od = __builtin_amdgcn_mfma_f32_32x32x16_bf16(AT_PK(l2, h2), pa2, od, 0, 0, 0);
;     od = __builtin_amdgcn_mfma_f32_32x32x16_bf16(AT_PK(l3, h3), pa3, od, 0, 0, 0);
;     ...
; }
; DI void pv_all_sm(f32x16* o, int vb, bf16x8 pa0, bf16x8 pa1, bf16x8 pa2, bf16x8 pa3, f32x16& p0, f32x16& p1, float& m_ref, f32x16& negm, float& alpha) {
;     pv_one<0>(o[0], vb, pa0, pa1, pa2, pa3);
;     float pmax = p0[0];
; #pragma unroll
;     for (int r = 1; r < 16; ++r) pmax = fmaxf(pmax, p0[r]);
;     pv_one<1>(o[1], vb, pa0, pa1, pa2, pa3);
; #pragma unroll
;     for (int r = 0; r < 16; ++r) pmax = fmaxf(pmax, p1[r]);
;     { auto rr = __builtin_amdgcn_permlane32_swap(__float_as_uint(pmax), __float_as_uint(pmax), false, false); pmax = fmaxf(__uint_as_float(rr[0]), __uint_as_float(rr[1])); }
;     pv_one<2>(o[2], vb, pa0, pa1, pa2, pa3);
;     alpha = 1.f;
;     if (__builtin_expect(!__all(pmax <= THRL), 0)) {
;         const float dl = fmaxf(pmax, 0.f); m_ref += dl; alpha = __builtin_amdgcn_exp2f(-dl);
; #pragma unroll
;         for (int r = 0; r < 16; ++r) { p0[r] -= dl; p1[r] -= dl; }
; #pragma unroll
;         for (int r = 0; r < 16; ++r) negm[r] = -m_ref;
;     }
;     pv_one<3>(o[3], vb, pa0, pa1, pa2, pa3);
; #pragma unroll
;     for (int r = 0; r < 16; ++r) p0[r] = __builtin_amdgcn_exp2f(p0[r]);
; }
.LBB4_704:
	s_lshl_b32 s67, s65, 14
	v_add_u32_e32 v186, s67, v253
	ds_read_b64_tr_b16 v[64:65], v186 offset:0
	ds_read_b64_tr_b16 v[66:67], v186 offset:0x100
	ds_read_b64_tr_b16 v[68:69], v186 offset:0x1000
	ds_read_b64_tr_b16 v[70:71], v186 offset:0x1100
	ds_read_b64_tr_b16 v[72:73], v186 offset:0x2000
	ds_read_b64_tr_b16 v[74:75], v186 offset:0x2100
	ds_read_b64_tr_b16 v[76:77], v186 offset:0x3000
	ds_read_b64_tr_b16 v[78:79], v186 offset:0x3100
	s_waitcnt lgkmcnt(0)
	v_mfma_f32_32x32x16_bf16 v[32:47], v[64:67], v[96:99], v[32:47]
	v_max_f32_e32 v64, v128, v129
	v_max3_f32 v64, v64, v130, v131
	v_max3_f32 v64, v64, v132, v133
	v_max3_f32 v64, v64, v134, v135
	v_max3_f32 v64, v64, v136, v137
	v_mfma_f32_32x32x16_bf16 v[32:47], v[68:71], v[108:111], v[32:47]
	v_max3_f32 v64, v64, v138, v139
	v_max3_f32 v66, v64, v140, v141
	ds_read_b64_tr_b16 v[64:65], v186 offset:0x200
	v_max3_f32 v180, v66, v142, v143
	ds_read_b64_tr_b16 v[66:67], v186 offset:0x300
	ds_read_b64_tr_b16 v[68:69], v186 offset:0x1200
	ds_read_b64_tr_b16 v[70:71], v186 offset:0x1300
	v_mfma_f32_32x32x16_bf16 v[32:47], v[72:75], v[100:103], v[32:47]
	ds_read_b64_tr_b16 v[72:73], v186 offset:0x2200
	ds_read_b64_tr_b16 v[74:75], v186 offset:0x2300
	ds_read_b64_tr_b16 v[214:215], v186 offset:0x3200
	ds_read_b64_tr_b16 v[216:217], v186 offset:0x3300
	s_waitcnt lgkmcnt(0)
	v_mfma_f32_32x32x16_bf16 v[32:47], v[76:79], v[104:107], v[32:47]
	v_mfma_f32_32x32x16_bf16 v[48:63], v[64:67], v[96:99], v[48:63]
	v_max3_f32 v76, v180, v112, v113
	v_max3_f32 v64, v76, v114, v115
	ds_read_b64_tr_b16 v[66:67], v186 offset:0x400
	v_max3_f32 v64, v64, v116, v117
	v_max3_f32 v64, v64, v118, v119
	v_max3_f32 v64, v64, v120, v121
	v_max3_f32 v64, v64, v122, v123
	v_mfma_f32_32x32x16_bf16 v[48:63], v[68:71], v[108:111], v[48:63]
	ds_read_b64_tr_b16 v[68:69], v186 offset:0x500
	ds_read_b64_tr_b16 v[70:71], v186 offset:0x1400
	v_max3_f32 v64, v64, v124, v125
	v_max3_f32 v64, v64, v126, v127
	v_mov_b32_e32 v65, v64
	s_nop 1
	v_permlane32_swap_b32_e32 v64, v65
	v_mfma_f32_32x32x16_bf16 v[48:63], v[72:75], v[100:103], v[48:63]
	ds_read_b64_tr_b16 v[72:73], v186 offset:0x1500
	ds_read_b64_tr_b16 v[74:75], v186 offset:0x2400
	ds_read_b64_tr_b16 v[76:77], v186 offset:0x2500
	ds_read_b64_tr_b16 v[218:219], v186 offset:0x3400
	ds_read_b64_tr_b16 v[220:221], v186 offset:0x3500
	s_waitcnt lgkmcnt(0)
	v_mfma_f32_32x32x16_bf16 v[48:63], v[214:217], v[104:107], v[48:63]
	ds_read_b64_tr_b16 v[214:215], v186 offset:0x600
	ds_read_b64_tr_b16 v[216:217], v186 offset:0x700
	ds_read_b64_tr_b16 v[222:223], v186 offset:0x2600
	ds_read_b64_tr_b16 v[224:225], v186 offset:0x2700
	ds_read_b64_tr_b16 v[226:227], v186 offset:0x3600
	ds_read_b64_tr_b16 v[228:229], v186 offset:0x3700
	v_max_f32_e32 v64, v64, v65
	v_mfma_f32_32x32x16_bf16 v[16:31], v[66:69], v[96:99], v[16:31]
	v_cmp_ge_f32_e32 vcc, s25, v64
	s_cmp_eq_u64 vcc, exec
	v_mfma_f32_32x32x16_bf16 v[16:31], v[70:73], v[108:111], v[16:31]
	v_mfma_f32_32x32x16_bf16 v[16:31], v[74:77], v[100:103], v[16:31]
	v_mfma_f32_32x32x16_bf16 v[16:31], v[218:221], v[104:107], v[16:31]
	s_cbranch_scc0 .LBB4_737
	v_mov_b32_e32 v180, 1.0
.LBB4_706:
	ds_read_b64_tr_b16 v[218:219], v186 offset:0x1600
	ds_read_b64_tr_b16 v[220:221], v186 offset:0x1700
	s_waitcnt lgkmcnt(0)
	v_mfma_f32_32x32x16_bf16 v[0:15], v[214:217], v[96:99], v[0:15]
	s_lshl_b32 s2, s64, 14
	s_add_i32 s2, s2, 0
	s_lshl_b32 s3, s64, 13
	v_add_u32_e32 v96, s2, v200
	s_sub_i32 s78, s2, s3
	s_waitcnt vmcnt(0)
	v_add_u32_e32 v97, s2, v201
	v_mfma_f32_32x32x16_bf16 v[0:15], v[218:221], v[108:111], v[0:15]
	ds_write_b128 v96, v[176:179]
	v_add_u32_e32 v96, s78, v202
	ds_write_b128 v97, v[172:175]
	ds_write_b128 v96, v[168:171] offset:49152
	s_andn2_b64 s[2:3], exec, s[34:35]
	s_andn2_b64 vcc, exec, s[34:35]
	v_mfma_f32_32x32x16_bf16 v[0:15], v[222:225], v[100:103], v[0:15]
	v_mfma_f32_32x32x16_bf16 v[0:15], v[226:229], v[104:107], v[0:15]
	s_cbranch_vccnz .LBB4_711
	v_med3_f32 v97, v160, -v255, v255
	v_med3_f32 v98, v164, -v255, v255
	v_cvt_scalef32_pk_fp8_f32 v99, v97, v98, s93
	v_med3_f32 v97, v161, -v255, v255
	v_med3_f32 v98, v165, -v255, v255
	v_cvt_scalef32_pk_fp8_f32 v100, v97, v98, s93
	v_med3_f32 v97, v162, -v255, v255
	v_med3_f32 v98, v166, -v255, v255
	s_bitcmp1_b32 s58, 0
	v_cvt_scalef32_pk_fp8_f32 v101, v97, v98, s93
	s_cselect_b32 s8, 0x1100, 0
	v_med3_f32 v97, v163, -v255, v255
	v_med3_f32 v98, v167, -v255, v255
	v_cmp_eq_u32_e32 vcc, 0, v181
	v_add_u32_e32 v96, s8, v191
	v_cvt_scalef32_pk_fp8_f32 v102, v97, v98, s93
	s_and_b64 vcc, exec, vcc
	s_and_b32 s34, s58, 31
	ds_write_b16 v96, v99
	ds_write_b16 v96, v100 offset:68
	ds_write_b16 v96, v101 offset:136
	ds_write_b16 v96, v102 offset:204
	s_cbranch_vccnz .LBB4_735
	s_lshl_b32 s8, s34, 7
	s_lshl_b32 s9, s58, 6
	s_and_b32 s8, s8, 0xf00
	s_and_b32 s9, s9, 64
	s_or_b32 s26, s8, s9
	s_cbranch_execnz .LBB4_710

; #define AT_SBAR() __builtin_amdgcn_sched_barrier(0)
; template <int OFF> DI s16x4 tr_read(int vb) { s16x4 r; asm volatile("ds_read_b64_tr_b16 %0, %1 offset:%2" : "=&v"(r) : "v"(vb), "i"(OFF) : "memory"); return r; }
; template <int D0> DI void pv_one(f32x16& od, int vb, bf16x8 pa0, bf16x8 pa1, bf16x8 pa2, bf16x8 pa3) {
;     const s16x4 l0 = tr_read<v_rd_off(D0, 0, 0)>(vb), h0 = tr_read<v_rd_off(D0, 0, 1)>(vb), l1 = tr_read<v_rd_off(D0, 1, 0)>(vb), h1 = tr_read<v_rd_off(D0, 1, 1)>(vb);
;     const s16x4 l2 = tr_read<v_rd_off(D0, 2, 0)>(vb), h2 = tr_read<v_rd_off(D0, 2, 1)>(vb), l3 = tr_read<v_rd_off(D0, 3, 0)>(vb), h3 = tr_read<v_rd_off(D0, 3, 1)>(vb);
;     asm volatile("s_waitcnt lgkmcnt(0)" ::: "memory"); AT_SBAR();
;     ...
;     od = __builtin_amdgcn_mfma_f32_32x32x16_bf16(AT_PK(l0, h0), pa0, od, 0, 0, 0);
;     od = __builtin_amdgcn_mfma_f32_32x32x16_bf16(AT_PK(l1, h1), pa1, od, 0, 0, 0);
;     od = __builtin_amdgcn_mfma_f32_32x32x16_bf16(AT_PK(l2, h2), pa2, od, 0, 0, 0);
;     od = __builtin_amdgcn_mfma_f32_32x32x16_bf16(AT_PK(l3, h3), pa3, od, 0, 0, 0);
;     ...
; }
; DI void pv_all_sm(f32x16* o, int vb, bf16x8 pa0, bf16x8 pa1, bf16x8 pa2, bf16x8 pa3, f32x16& p0, f32x16& p1, float& m_ref, f32x16& negm, float& alpha) {
;     pv_one<0>(o[0], vb, pa0, pa1, pa2, pa3);
;     float pmax = p0[0];
; #pragma unroll
;     for (int r = 1; r < 16; ++r) pmax = fmaxf(pmax, p0[r]);
;     pv_one<1>(o[1], vb, pa0, pa1, pa2, pa3);
; #pragma unroll
;     for (int r = 0; r < 16; ++r) pmax = fmaxf(pmax, p1[r]);
;     { auto rr = __builtin_amdgcn_permlane32_swap(__float_as_uint(pmax), __float_as_uint(pmax), false, false); pmax = fmaxf(__uint_as_float(rr[0]), __uint_as_float(rr[1])); }
;     pv_one<2>(o[2], vb, pa0, pa1, pa2, pa3);
;     alpha = 1.f;
;     if (__builtin_expect(!__all(pmax <= THRL), 0)) {
;         const float dl = fmaxf(pmax, 0.f); m_ref += dl; alpha = __builtin_amdgcn_exp2f(-dl);
; #pragma unroll
;         for (int r = 0; r < 16; ++r) { p0[r] -= dl; p1[r] -= dl; }
; #pragma unroll
;         for (int r = 0; r < 16; ++r) negm[r] = -m_ref;
;     }
;     pv_one<3>(o[3], vb, pa0, pa1, pa2, pa3);
; #pragma unroll
;     for (int r = 0; r < 16; ++r) p0[r] = __builtin_amdgcn_exp2f(p0[r]);
; }
.LBB4_725:
	v_lshl_add_u32 v215, s66, 14, v253
	ds_read_b64_tr_b16 v[216:217], v215 offset:0
	ds_read_b64_tr_b16 v[218:219], v215 offset:0x100
	ds_read_b64_tr_b16 v[220:221], v215 offset:0x1000
	ds_read_b64_tr_b16 v[222:223], v215 offset:0x1100
	ds_read_b64_tr_b16 v[224:225], v215 offset:0x2000
	ds_read_b64_tr_b16 v[226:227], v215 offset:0x2100
	ds_read_b64_tr_b16 v[228:229], v215 offset:0x3000
	ds_read_b64_tr_b16 v[230:231], v215 offset:0x3100
	s_waitcnt lgkmcnt(0)
	v_mfma_f32_32x32x16_bf16 v[32:47], v[216:219], v[120:123], v[32:47]
	v_max_f32_e32 v186, v128, v129
	ds_read_b64_tr_b16 v[216:217], v215 offset:0x200
	ds_read_b64_tr_b16 v[218:219], v215 offset:0x300
	v_max3_f32 v186, v186, v130, v131
	v_max3_f32 v186, v186, v132, v133
	v_mfma_f32_32x32x16_bf16 v[32:47], v[220:223], v[124:127], v[32:47]
	ds_read_b64_tr_b16 v[220:221], v215 offset:0x1200
	ds_read_b64_tr_b16 v[222:223], v215 offset:0x1300
	v_max3_f32 v186, v186, v134, v135
	v_max3_f32 v186, v186, v136, v137
	v_max3_f32 v186, v186, v138, v139
	v_max3_f32 v186, v186, v140, v141
	v_max3_f32 v186, v186, v142, v143
	v_mfma_f32_32x32x16_bf16 v[32:47], v[224:227], v[112:115], v[32:47]
	ds_read_b64_tr_b16 v[224:225], v215 offset:0x2200
	ds_read_b64_tr_b16 v[226:227], v215 offset:0x2300
	ds_read_b64_tr_b16 v[232:233], v215 offset:0x3200
	ds_read_b64_tr_b16 v[234:235], v215 offset:0x3300
	s_waitcnt lgkmcnt(0)
	v_mfma_f32_32x32x16_bf16 v[32:47], v[228:231], v[116:119], v[32:47]
	v_mfma_f32_32x32x16_bf16 v[48:63], v[216:219], v[120:123], v[48:63]
	v_max3_f32 v186, v186, v96, v97
	v_max3_f32 v186, v186, v98, v99
	ds_read_b64_tr_b16 v[218:219], v215 offset:0x400
	v_max3_f32 v186, v186, v100, v101
	v_max3_f32 v186, v186, v102, v103
	v_max3_f32 v186, v186, v104, v105
	v_max3_f32 v186, v186, v106, v107
	v_mfma_f32_32x32x16_bf16 v[48:63], v[220:223], v[124:127], v[48:63]
	ds_read_b64_tr_b16 v[220:221], v215 offset:0x500
	ds_read_b64_tr_b16 v[222:223], v215 offset:0x1400
	v_max3_f32 v186, v186, v108, v109
	v_max3_f32 v186, v186, v110, v111
	v_mov_b32_e32 v216, v186
	s_nop 1
	v_permlane32_swap_b32_e32 v186, v216
	v_mfma_f32_32x32x16_bf16 v[48:63], v[224:227], v[112:115], v[48:63]
	ds_read_b64_tr_b16 v[224:225], v215 offset:0x1500
	ds_read_b64_tr_b16 v[226:227], v215 offset:0x2400
	ds_read_b64_tr_b16 v[228:229], v215 offset:0x2500
	ds_read_b64_tr_b16 v[236:237], v215 offset:0x3400
	ds_read_b64_tr_b16 v[238:239], v215 offset:0x3500
	s_waitcnt lgkmcnt(0)
	v_mfma_f32_32x32x16_bf16 v[48:63], v[232:235], v[116:119], v[48:63]
	ds_read_b64_tr_b16 v[230:231], v215 offset:0x3700
	v_max_f32_e32 v216, v186, v216
	v_mfma_f32_32x32x16_bf16 v[16:31], v[218:221], v[120:123], v[16:31]
	v_cmp_ge_f32_e32 vcc, s25, v216
	s_cmp_eq_u64 vcc, exec
	v_mov_b32_e32 v186, 1.0
	v_mfma_f32_32x32x16_bf16 v[16:31], v[222:225], v[124:127], v[16:31]
	v_mfma_f32_32x32x16_bf16 v[16:31], v[226:229], v[112:115], v[16:31]
	v_mfma_f32_32x32x16_bf16 v[16:31], v[236:239], v[116:119], v[16:31]
	s_cbranch_scc0 .LBB4_738
.LBB4_726:
	ds_read_b64_tr_b16 v[216:217], v215 offset:0x600
	ds_read_b64_tr_b16 v[218:219], v215 offset:0x700
	ds_read_b64_tr_b16 v[220:221], v215 offset:0x1600
	ds_read_b64_tr_b16 v[222:223], v215 offset:0x1700
	ds_read_b64_tr_b16 v[224:225], v215 offset:0x2600
	ds_read_b64_tr_b16 v[226:227], v215 offset:0x2700
	ds_read_b64_tr_b16 v[228:229], v215 offset:0x3600
	s_waitcnt lgkmcnt(0)
	v_mfma_f32_32x32x16_bf16 v[0:15], v[216:219], v[120:123], v[0:15]
	s_add_i32 s2, s67, 0
	v_add_u32_e32 v120, s2, v200
	s_waitcnt vmcnt(0)
	ds_write_b128 v120, v[176:179]
	s_mov_b32 s26, 0
	s_andn2_b64 vcc, exec, s[34:35]
	v_mfma_f32_32x32x16_bf16 v[0:15], v[220:223], v[124:127], v[0:15]
	v_mfma_f32_32x32x16_bf16 v[0:15], v[224:227], v[112:115], v[0:15]
	v_add_u32_e32 v112, s2, v201
	ds_write_b128 v112, v[172:175]
	v_lshl_add_u32 v112, s65, 13, v203
	ds_write_b128 v112, v[168:171] offset:49152
	s_andn2_b64 s[2:3], exec, s[34:35]
	v_mfma_f32_32x32x16_bf16 v[0:15], v[228:231], v[116:119], v[0:15]
	s_cbranch_vccnz .LBB4_731
	v_med3_f32 v113, v160, -v255, v255
	v_med3_f32 v114, v164, -v255, v255
	v_cvt_scalef32_pk_fp8_f32 v115, v113, v114, s93
	v_med3_f32 v113, v161, -v255, v255
	v_med3_f32 v114, v165, -v255, v255
	v_cvt_scalef32_pk_fp8_f32 v116, v113, v114, s93
	v_med3_f32 v113, v162, -v255, v255
	v_med3_f32 v114, v166, -v255, v255
	s_bitcmp1_b32 s58, 0
	v_cvt_scalef32_pk_fp8_f32 v117, v113, v114, s93
	s_cselect_b32 s8, 0x1100, 0
	v_med3_f32 v113, v163, -v255, v255
	v_med3_f32 v114, v167, -v255, v255
	v_cmp_eq_u32_e32 vcc, 0, v181
	v_add_u32_e32 v112, s8, v191
	v_cvt_scalef32_pk_fp8_f32 v118, v113, v114, s93
	s_and_b64 vcc, exec, vcc
	s_and_b32 s37, s58, 31
	ds_write_b16 v112, v115
	ds_write_b16 v112, v116 offset:68
	ds_write_b16 v112, v117 offset:136
	ds_write_b16 v112, v118 offset:204
	s_cbranch_vccnz .LBB4_736
	s_lshl_b32 s8, s37, 7
	s_lshl_b32 s9, s58, 6
	s_and_b32 s8, s8, 0xf00
	s_and_b32 s9, s9, 64
	s_or_b32 s26, s8, s9
	s_cbranch_execnz .LBB4_730

; #define AT_SBAR() __builtin_amdgcn_sched_barrier(0)
; template <int OFF> DI s16x4 tr_read(int vb) { s16x4 r; asm volatile("ds_read_b64_tr_b16 %0, %1 offset:%2" : "=&v"(r) : "v"(vb), "i"(OFF) : "memory"); return r; }
; template <int D0> DI void pv_one(f32x16& od, int vb, bf16x8 pa0, bf16x8 pa1, bf16x8 pa2, bf16x8 pa3) {
;     const s16x4 l0 = tr_read<v_rd_off(D0, 0, 0)>(vb), h0 = tr_read<v_rd_off(D0, 0, 1)>(vb), l1 = tr_read<v_rd_off(D0, 1, 0)>(vb), h1 = tr_read<v_rd_off(D0, 1, 1)>(vb);
;     const s16x4 l2 = tr_read<v_rd_off(D0, 2, 0)>(vb), h2 = tr_read<v_rd_off(D0, 2, 1)>(vb), l3 = tr_read<v_rd_off(D0, 3, 0)>(vb), h3 = tr_read<v_rd_off(D0, 3, 1)>(vb);
;     asm volatile("s_waitcnt lgkmcnt(0)" ::: "memory"); AT_SBAR();
;     ...
;     od = __builtin_amdgcn_mfma_f32_32x32x16_bf16(AT_PK(l0, h0), pa0, od, 0, 0, 0);
;     od = __builtin_amdgcn_mfma_f32_32x32x16_bf16(AT_PK(l1, h1), pa1, od, 0, 0, 0);
;     od = __builtin_amdgcn_mfma_f32_32x32x16_bf16(AT_PK(l2, h2), pa2, od, 0, 0, 0);
;     od = __builtin_amdgcn_mfma_f32_32x32x16_bf16(AT_PK(l3, h3), pa3, od, 0, 0, 0);
;     ...
; }
; DI void pv_all_sm(f32x16* o, int vb, bf16x8 pa0, bf16x8 pa1, bf16x8 pa2, bf16x8 pa3, f32x16& p0, f32x16& p1, float& m_ref, f32x16& negm, float& alpha) {
;     pv_one<0>(o[0], vb, pa0, pa1, pa2, pa3);
;     float pmax = p0[0];
; #pragma unroll
;     for (int r = 1; r < 16; ++r) pmax = fmaxf(pmax, p0[r]);
;     pv_one<1>(o[1], vb, pa0, pa1, pa2, pa3);
; #pragma unroll
;     for (int r = 0; r < 16; ++r) pmax = fmaxf(pmax, p1[r]);
;     { auto rr = __builtin_amdgcn_permlane32_swap(__float_as_uint(pmax), __float_as_uint(pmax), false, false); pmax = fmaxf(__uint_as_float(rr[0]), __uint_as_float(rr[1])); }
;     pv_one<2>(o[2], vb, pa0, pa1, pa2, pa3);
;     alpha = 1.f;
;     if (__builtin_expect(!__all(pmax <= THRL), 0)) {
;         const float dl = fmaxf(pmax, 0.f); m_ref += dl; alpha = __builtin_amdgcn_exp2f(-dl);
; #pragma unroll
;         for (int r = 0; r < 16; ++r) { p0[r] -= dl; p1[r] -= dl; }
; #pragma unroll
;         for (int r = 0; r < 16; ++r) negm[r] = -m_ref;
;     }
;     pv_one<3>(o[3], vb, pa0, pa1, pa2, pa3);
; #pragma unroll
;     for (int r = 0; r < 16; ++r) p0[r] = __builtin_amdgcn_exp2f(p0[r]);
; }
.LBB4_777:
	s_lshl_b32 s31, s29, 14
	v_add_u32_e32 v182, s31, v253
	ds_read_b64_tr_b16 v[64:65], v182 offset:0
	ds_read_b64_tr_b16 v[66:67], v182 offset:0x100
	ds_read_b64_tr_b16 v[68:69], v182 offset:0x1000
	ds_read_b64_tr_b16 v[70:71], v182 offset:0x1100
	ds_read_b64_tr_b16 v[72:73], v182 offset:0x2000
	ds_read_b64_tr_b16 v[74:75], v182 offset:0x2100
	ds_read_b64_tr_b16 v[76:77], v182 offset:0x3000
	ds_read_b64_tr_b16 v[78:79], v182 offset:0x3100
	s_waitcnt lgkmcnt(0)
	v_mfma_f32_32x32x16_bf16 v[48:63], v[64:67], v[96:99], v[48:63]
	v_max_f32_e32 v64, v128, v129
	v_max3_f32 v64, v64, v130, v131
	v_max3_f32 v64, v64, v132, v133
	v_max3_f32 v64, v64, v134, v135
	v_max3_f32 v64, v64, v136, v137
	v_mfma_f32_32x32x16_bf16 v[48:63], v[68:71], v[108:111], v[48:63]
	v_max3_f32 v64, v64, v138, v139
	v_max3_f32 v66, v64, v140, v141
	ds_read_b64_tr_b16 v[64:65], v182 offset:0x200
	v_max3_f32 v180, v66, v142, v143
	ds_read_b64_tr_b16 v[66:67], v182 offset:0x300
	ds_read_b64_tr_b16 v[68:69], v182 offset:0x1200
	ds_read_b64_tr_b16 v[70:71], v182 offset:0x1300
	v_mfma_f32_32x32x16_bf16 v[48:63], v[72:75], v[100:103], v[48:63]
	ds_read_b64_tr_b16 v[72:73], v182 offset:0x2200
	ds_read_b64_tr_b16 v[74:75], v182 offset:0x2300
	ds_read_b64_tr_b16 v[218:219], v182 offset:0x3200
	ds_read_b64_tr_b16 v[220:221], v182 offset:0x3300
	s_waitcnt lgkmcnt(0)
	v_mfma_f32_32x32x16_bf16 v[48:63], v[76:79], v[104:107], v[48:63]
	ds_read_b64_tr_b16 v[226:227], v182 offset:0x2600
	ds_read_b64_tr_b16 v[228:229], v182 offset:0x2700
	ds_read_b64_tr_b16 v[230:231], v182 offset:0x3600
	ds_read_b64_tr_b16 v[232:233], v182 offset:0x3700
	v_mfma_f32_32x32x16_bf16 v[32:47], v[64:67], v[96:99], v[32:47]
	v_max3_f32 v76, v180, v112, v113
	v_max3_f32 v64, v76, v114, v115
	ds_read_b64_tr_b16 v[66:67], v182 offset:0x400
	v_max3_f32 v64, v64, v116, v117
	v_max3_f32 v64, v64, v118, v119
	v_max3_f32 v64, v64, v120, v121
	v_max3_f32 v64, v64, v122, v123
	v_mfma_f32_32x32x16_bf16 v[32:47], v[68:71], v[108:111], v[32:47]
	ds_read_b64_tr_b16 v[68:69], v182 offset:0x500
	ds_read_b64_tr_b16 v[70:71], v182 offset:0x1400
	v_max3_f32 v64, v64, v124, v125
	v_max3_f32 v64, v64, v126, v127
	v_mov_b32_e32 v65, v64
	s_nop 1
	v_permlane32_swap_b32_e32 v64, v65
	v_mfma_f32_32x32x16_bf16 v[32:47], v[72:75], v[100:103], v[32:47]
	ds_read_b64_tr_b16 v[72:73], v182 offset:0x1500
	ds_read_b64_tr_b16 v[74:75], v182 offset:0x2400
	ds_read_b64_tr_b16 v[76:77], v182 offset:0x2500
	ds_read_b64_tr_b16 v[222:223], v182 offset:0x3400
	ds_read_b64_tr_b16 v[224:225], v182 offset:0x3500
	s_waitcnt lgkmcnt(0)
	v_mfma_f32_32x32x16_bf16 v[32:47], v[218:221], v[104:107], v[32:47]
	v_max_f32_e32 v64, v64, v65
	v_mfma_f32_32x32x16_bf16 v[16:31], v[66:69], v[96:99], v[16:31]
	v_cmp_ge_f32_e32 vcc, s26, v64
	s_cmp_eq_u64 vcc, exec
	v_mfma_f32_32x32x16_bf16 v[16:31], v[70:73], v[108:111], v[16:31]
	v_mfma_f32_32x32x16_bf16 v[16:31], v[74:77], v[100:103], v[16:31]
	v_mfma_f32_32x32x16_bf16 v[16:31], v[222:225], v[104:107], v[16:31]
	s_cbranch_scc0 .LBB4_810
	v_mov_b32_e32 v180, 1.0
.LBB4_779:
	ds_read_b64_tr_b16 v[218:219], v182 offset:0x600
	ds_read_b64_tr_b16 v[220:221], v182 offset:0x700
	ds_read_b64_tr_b16 v[222:223], v182 offset:0x1600
	ds_read_b64_tr_b16 v[224:225], v182 offset:0x1700
	s_waitcnt lgkmcnt(0)
	v_mfma_f32_32x32x16_bf16 v[0:15], v[218:221], v[96:99], v[0:15]
	s_lshl_b32 s2, s15, 14
	s_add_i32 s2, s2, 0
	s_lshl_b32 s3, s15, 13
	v_add_u32_e32 v96, s2, v203
	s_sub_i32 s65, s2, s3
	s_waitcnt vmcnt(0)
	v_add_u32_e32 v97, s2, v204
	v_mfma_f32_32x32x16_bf16 v[0:15], v[222:225], v[108:111], v[0:15]
	ds_write_b128 v96, v[176:179]
	v_add_u32_e32 v96, s65, v205
	ds_write_b128 v97, v[172:175]
	ds_write_b128 v96, v[168:171] offset:49152
	s_andn2_b64 s[2:3], exec, s[22:23]
	s_andn2_b64 vcc, exec, s[22:23]
	v_mfma_f32_32x32x16_bf16 v[0:15], v[226:229], v[100:103], v[0:15]
	v_mfma_f32_32x32x16_bf16 v[0:15], v[230:233], v[104:107], v[0:15]
	s_cbranch_vccnz .LBB4_784
	v_med3_f32 v97, v160, -v255, v255
	v_med3_f32 v98, v164, -v255, v255
	v_cvt_scalef32_pk_fp8_f32 v99, v97, v98, s93
	v_med3_f32 v97, v161, -v255, v255
	v_med3_f32 v98, v165, -v255, v255
	v_cvt_scalef32_pk_fp8_f32 v100, v97, v98, s93
	v_med3_f32 v97, v162, -v255, v255
	v_med3_f32 v98, v166, -v255, v255
	s_bitcmp1_b32 s58, 0
	v_cvt_scalef32_pk_fp8_f32 v101, v97, v98, s93
	s_cselect_b32 s8, 0x1100, 0
	v_med3_f32 v97, v163, -v255, v255
	v_med3_f32 v98, v167, -v255, v255
	v_cmp_eq_u32_e32 vcc, 0, v181
	v_add_u32_e32 v96, s8, v195
	v_cvt_scalef32_pk_fp8_f32 v102, v97, v98, s93
	s_and_b64 vcc, exec, vcc
	s_and_b32 s22, s58, 31
	ds_write_b16 v96, v99
	ds_write_b16 v96, v100 offset:68
	ds_write_b16 v96, v101 offset:136
	ds_write_b16 v96, v102 offset:204
	s_cbranch_vccnz .LBB4_808
	s_lshl_b32 s8, s22, 7
	s_lshl_b32 s9, s58, 6
	s_and_b32 s8, s8, 0xf00
	s_and_b32 s9, s9, 64
	s_or_b32 s20, s8, s9
	s_cbranch_execnz .LBB4_783

; #define AT_SBAR() __builtin_amdgcn_sched_barrier(0)
; template <int OFF> DI s16x4 tr_read(int vb) { s16x4 r; asm volatile("ds_read_b64_tr_b16 %0, %1 offset:%2" : "=&v"(r) : "v"(vb), "i"(OFF) : "memory"); return r; }
; template <int D0> DI void pv_one(f32x16& od, int vb, bf16x8 pa0, bf16x8 pa1, bf16x8 pa2, bf16x8 pa3) {
;     const s16x4 l0 = tr_read<v_rd_off(D0, 0, 0)>(vb), h0 = tr_read<v_rd_off(D0, 0, 1)>(vb), l1 = tr_read<v_rd_off(D0, 1, 0)>(vb), h1 = tr_read<v_rd_off(D0, 1, 1)>(vb);
;     const s16x4 l2 = tr_read<v_rd_off(D0, 2, 0)>(vb), h2 = tr_read<v_rd_off(D0, 2, 1)>(vb), l3 = tr_read<v_rd_off(D0, 3, 0)>(vb), h3 = tr_read<v_rd_off(D0, 3, 1)>(vb);
;     asm volatile("s_waitcnt lgkmcnt(0)" ::: "memory"); AT_SBAR();
;     ...
;     od = __builtin_amdgcn_mfma_f32_32x32x16_bf16(AT_PK(l0, h0), pa0, od, 0, 0, 0);
;     od = __builtin_amdgcn_mfma_f32_32x32x16_bf16(AT_PK(l1, h1), pa1, od, 0, 0, 0);
;     od = __builtin_amdgcn_mfma_f32_32x32x16_bf16(AT_PK(l2, h2), pa2, od, 0, 0, 0);
;     od = __builtin_amdgcn_mfma_f32_32x32x16_bf16(AT_PK(l3, h3), pa3, od, 0, 0, 0);
;     ...
; }
; DI void pv_all_sm(f32x16* o, int vb, bf16x8 pa0, bf16x8 pa1, bf16x8 pa2, bf16x8 pa3, f32x16& p0, f32x16& p1, float& m_ref, f32x16& negm, float& alpha) {
;     pv_one<0>(o[0], vb, pa0, pa1, pa2, pa3);
;     float pmax = p0[0];
; #pragma unroll
;     for (int r = 1; r < 16; ++r) pmax = fmaxf(pmax, p0[r]);
;     pv_one<1>(o[1], vb, pa0, pa1, pa2, pa3);
; #pragma unroll
;     for (int r = 0; r < 16; ++r) pmax = fmaxf(pmax, p1[r]);
;     { auto rr = __builtin_amdgcn_permlane32_swap(__float_as_uint(pmax), __float_as_uint(pmax), false, false); pmax = fmaxf(__uint_as_float(rr[0]), __uint_as_float(rr[1])); }
;     pv_one<2>(o[2], vb, pa0, pa1, pa2, pa3);
;     alpha = 1.f;
;     if (__builtin_expect(!__all(pmax <= THRL), 0)) {
;         const float dl = fmaxf(pmax, 0.f); m_ref += dl; alpha = __builtin_amdgcn_exp2f(-dl);
; #pragma unroll
;         for (int r = 0; r < 16; ++r) { p0[r] -= dl; p1[r] -= dl; }
; #pragma unroll
;         for (int r = 0; r < 16; ++r) negm[r] = -m_ref;
;     }
;     pv_one<3>(o[3], vb, pa0, pa1, pa2, pa3);
; #pragma unroll
;     for (int r = 0; r < 16; ++r) p0[r] = __builtin_amdgcn_exp2f(p0[r]);
; }
.LBB4_798:
	v_lshl_add_u32 v219, s30, 14, v253
	ds_read_b64_tr_b16 v[220:221], v219 offset:0
	ds_read_b64_tr_b16 v[222:223], v219 offset:0x100
	ds_read_b64_tr_b16 v[224:225], v219 offset:0x1000
	ds_read_b64_tr_b16 v[226:227], v219 offset:0x1100
	ds_read_b64_tr_b16 v[228:229], v219 offset:0x2000
	ds_read_b64_tr_b16 v[230:231], v219 offset:0x2100
	ds_read_b64_tr_b16 v[232:233], v219 offset:0x3000
	ds_read_b64_tr_b16 v[234:235], v219 offset:0x3100
	s_waitcnt lgkmcnt(0)
	v_mfma_f32_32x32x16_bf16 v[48:63], v[220:223], v[120:123], v[48:63]
	v_max_f32_e32 v182, v128, v129
	ds_read_b64_tr_b16 v[220:221], v219 offset:0x200
	ds_read_b64_tr_b16 v[222:223], v219 offset:0x300
	v_max3_f32 v182, v182, v130, v131
	v_max3_f32 v182, v182, v132, v133
	v_mfma_f32_32x32x16_bf16 v[48:63], v[224:227], v[124:127], v[48:63]
	ds_read_b64_tr_b16 v[224:225], v219 offset:0x1200
	ds_read_b64_tr_b16 v[226:227], v219 offset:0x1300
	v_max3_f32 v182, v182, v134, v135
	v_max3_f32 v182, v182, v136, v137
	v_max3_f32 v182, v182, v138, v139
	v_max3_f32 v182, v182, v140, v141
	v_max3_f32 v182, v182, v142, v143
	v_mfma_f32_32x32x16_bf16 v[48:63], v[228:231], v[112:115], v[48:63]
	ds_read_b64_tr_b16 v[228:229], v219 offset:0x2200
	ds_read_b64_tr_b16 v[230:231], v219 offset:0x2300
	ds_read_b64_tr_b16 v[236:237], v219 offset:0x3200
	ds_read_b64_tr_b16 v[238:239], v219 offset:0x3300
	s_waitcnt lgkmcnt(0)
	v_mfma_f32_32x32x16_bf16 v[48:63], v[232:235], v[116:119], v[48:63]
	ds_read_b64_tr_b16 v[234:235], v219 offset:0x3700
	v_mfma_f32_32x32x16_bf16 v[32:47], v[220:223], v[120:123], v[32:47]
	v_max3_f32 v182, v182, v96, v97
	v_max3_f32 v182, v182, v98, v99
	ds_read_b64_tr_b16 v[222:223], v219 offset:0x400
	v_max3_f32 v182, v182, v100, v101
	v_max3_f32 v182, v182, v102, v103
	v_max3_f32 v182, v182, v104, v105
	v_max3_f32 v182, v182, v106, v107
	v_mfma_f32_32x32x16_bf16 v[32:47], v[224:227], v[124:127], v[32:47]
	ds_read_b64_tr_b16 v[224:225], v219 offset:0x500
	ds_read_b64_tr_b16 v[226:227], v219 offset:0x1400
	v_max3_f32 v182, v182, v108, v109
	v_max3_f32 v182, v182, v110, v111
	v_mov_b32_e32 v220, v182
	s_nop 1
	v_permlane32_swap_b32_e32 v182, v220
	v_mfma_f32_32x32x16_bf16 v[32:47], v[228:231], v[112:115], v[32:47]
	ds_read_b64_tr_b16 v[228:229], v219 offset:0x1500
	ds_read_b64_tr_b16 v[230:231], v219 offset:0x2400
	ds_read_b64_tr_b16 v[232:233], v219 offset:0x2500
	ds_read_b64_tr_b16 v[240:241], v219 offset:0x3400
	ds_read_b64_tr_b16 v[242:243], v219 offset:0x3500
	s_waitcnt lgkmcnt(0)
	v_mfma_f32_32x32x16_bf16 v[32:47], v[236:239], v[116:119], v[32:47]
	v_max_f32_e32 v220, v182, v220
	v_mfma_f32_32x32x16_bf16 v[16:31], v[222:225], v[120:123], v[16:31]
	v_cmp_ge_f32_e32 vcc, s26, v220
	s_cmp_eq_u64 vcc, exec
	v_mov_b32_e32 v182, 1.0
	v_mfma_f32_32x32x16_bf16 v[16:31], v[226:229], v[124:127], v[16:31]
	v_mfma_f32_32x32x16_bf16 v[16:31], v[230:233], v[112:115], v[16:31]
	v_mfma_f32_32x32x16_bf16 v[16:31], v[240:243], v[116:119], v[16:31]
	s_cbranch_scc0 .LBB4_811
.LBB4_799:
	ds_read_b64_tr_b16 v[220:221], v219 offset:0x600
	ds_read_b64_tr_b16 v[222:223], v219 offset:0x700
	ds_read_b64_tr_b16 v[224:225], v219 offset:0x1600
	ds_read_b64_tr_b16 v[226:227], v219 offset:0x1700
	ds_read_b64_tr_b16 v[228:229], v219 offset:0x2600
	ds_read_b64_tr_b16 v[230:231], v219 offset:0x2700
	ds_read_b64_tr_b16 v[232:233], v219 offset:0x3600
	s_waitcnt lgkmcnt(0)
	v_mfma_f32_32x32x16_bf16 v[0:15], v[220:223], v[120:123], v[0:15]
	s_add_i32 s2, s31, 0
	v_add_u32_e32 v120, s2, v203
	s_waitcnt vmcnt(0)
	ds_write_b128 v120, v[176:179]
	s_mov_b32 s20, 0
	s_andn2_b64 vcc, exec, s[22:23]
	v_mfma_f32_32x32x16_bf16 v[0:15], v[224:227], v[124:127], v[0:15]
	v_mfma_f32_32x32x16_bf16 v[0:15], v[228:231], v[112:115], v[0:15]
	v_add_u32_e32 v112, s2, v204
	ds_write_b128 v112, v[172:175]
	v_lshl_add_u32 v112, s29, 13, v206
	ds_write_b128 v112, v[168:171] offset:49152
	s_andn2_b64 s[2:3], exec, s[22:23]
	v_mfma_f32_32x32x16_bf16 v[0:15], v[232:235], v[116:119], v[0:15]
	s_cbranch_vccnz .LBB4_804
	v_med3_f32 v113, v160, -v255, v255
	v_med3_f32 v114, v164, -v255, v255
	v_cvt_scalef32_pk_fp8_f32 v115, v113, v114, s93
	v_med3_f32 v113, v161, -v255, v255
	v_med3_f32 v114, v165, -v255, v255
	v_cvt_scalef32_pk_fp8_f32 v116, v113, v114, s93
	v_med3_f32 v113, v162, -v255, v255
	v_med3_f32 v114, v166, -v255, v255
	s_bitcmp1_b32 s58, 0
	v_cvt_scalef32_pk_fp8_f32 v117, v113, v114, s93
	s_cselect_b32 s8, 0x1100, 0
	v_med3_f32 v113, v163, -v255, v255
	v_med3_f32 v114, v167, -v255, v255
	v_cmp_eq_u32_e32 vcc, 0, v181
	v_add_u32_e32 v112, s8, v195
	v_cvt_scalef32_pk_fp8_f32 v118, v113, v114, s93
	s_and_b64 vcc, exec, vcc
	s_and_b32 s24, s58, 31
	ds_write_b16 v112, v115
	ds_write_b16 v112, v116 offset:68
	ds_write_b16 v112, v117 offset:136
	ds_write_b16 v112, v118 offset:204
	s_cbranch_vccnz .LBB4_809
	s_lshl_b32 s8, s24, 7
	s_lshl_b32 s9, s58, 6
	s_and_b32 s8, s8, 0xf00
	s_and_b32 s9, s9, 64
	s_or_b32 s20, s8, s9
	s_cbranch_execnz .LBB4_803

; #define AT_SBAR() __builtin_amdgcn_sched_barrier(0)
; template <int D0> DI void pv_one(f32x16& od, int vb, bf16x8 pa0, bf16x8 pa1, bf16x8 pa2, bf16x8 pa3) {
;     const s16x4 l0 = tr_read<v_rd_off(D0, 0, 0)>(vb), h0 = tr_read<v_rd_off(D0, 0, 1)>(vb), l1 = tr_read<v_rd_off(D0, 1, 0)>(vb), h1 = tr_read<v_rd_off(D0, 1, 1)>(vb);
;     const s16x4 l2 = tr_read<v_rd_off(D0, 2, 0)>(vb), h2 = tr_read<v_rd_off(D0, 2, 1)>(vb), l3 = tr_read<v_rd_off(D0, 3, 0)>(vb), h3 = tr_read<v_rd_off(D0, 3, 1)>(vb);
;     asm volatile("s_waitcnt lgkmcnt(0)" ::: "memory"); AT_SBAR();
;     ...
;     od = __builtin_amdgcn_mfma_f32_32x32x16_bf16(AT_PK(l0, h0), pa0, od, 0, 0, 0);
;     od = __builtin_amdgcn_mfma_f32_32x32x16_bf16(AT_PK(l1, h1), pa1, od, 0, 0, 0);
;     od = __builtin_amdgcn_mfma_f32_32x32x16_bf16(AT_PK(l2, h2), pa2, od, 0, 0, 0);
;     od = __builtin_amdgcn_mfma_f32_32x32x16_bf16(AT_PK(l3, h3), pa3, od, 0, 0, 0);
;     ...
; }
; DI void pv_all_sm(f32x16* o, int vb, bf16x8 pa0, bf16x8 pa1, bf16x8 pa2, bf16x8 pa3, f32x16& p0, f32x16& p1, float& m_ref, f32x16& negm, float& alpha) {
;     pv_one<0>(o[0], vb, pa0, pa1, pa2, pa3);
;     float pmax = p0[0];
; #pragma unroll
;     for (int r = 1; r < 16; ++r) pmax = fmaxf(pmax, p0[r]);
;     pv_one<1>(o[1], vb, pa0, pa1, pa2, pa3);
; #pragma unroll
;     for (int r = 0; r < 16; ++r) pmax = fmaxf(pmax, p1[r]);
;     { auto rr = __builtin_amdgcn_permlane32_swap(__float_as_uint(pmax), __float_as_uint(pmax), false, false); pmax = fmaxf(__uint_as_float(rr[0]), __uint_as_float(rr[1])); }
;     pv_one<2>(o[2], vb, pa0, pa1, pa2, pa3);
;     alpha = 1.f;
;     if (__builtin_expect(!__all(pmax <= THRL), 0)) {
;         const float dl = fmaxf(pmax, 0.f); m_ref += dl; alpha = __builtin_amdgcn_exp2f(-dl);
; #pragma unroll
;         for (int r = 0; r < 16; ++r) { p0[r] -= dl; p1[r] -= dl; }
; #pragma unroll
;         for (int r = 0; r < 16; ++r) negm[r] = -m_ref;
;     }
;     pv_one<3>(o[3], vb, pa0, pa1, pa2, pa3);
; #pragma unroll
;     for (int r = 0; r < 16; ++r) p0[r] = __builtin_amdgcn_exp2f(p0[r]);
; }
; DI void attn_pass(const Frame& F, CvRide& cv, const bf16_t* __restrict__ Qb, const bf16_t* __restrict__ Kh, const bf16_t* __restrict__ Vh, char* lds, f32x16 (&o)[4], float& l_out, const int wave_s) {
;     ...
;     const unsigned cv_ldo = (unsigned)(((tid >> 4) * 2 * 2048 + (tid & 15) * 4) * 4), cv_sto = (unsigned)((tid >> 3) * 2048 + 8 * (tid & 7));
.LBB4_851:
	s_lshl_b32 s65, s63, 14
	v_add_u32_e32 v182, s65, v253
	ds_read_b64_tr_b16 v[64:65], v182 offset:0
	ds_read_b64_tr_b16 v[66:67], v182 offset:0x100
	ds_read_b64_tr_b16 v[68:69], v182 offset:0x1000
	ds_read_b64_tr_b16 v[70:71], v182 offset:0x1100
	ds_read_b64_tr_b16 v[72:73], v182 offset:0x2000
	ds_read_b64_tr_b16 v[74:75], v182 offset:0x2100
	ds_read_b64_tr_b16 v[76:77], v182 offset:0x3000
	ds_read_b64_tr_b16 v[78:79], v182 offset:0x3100
	s_waitcnt lgkmcnt(0)
	v_mfma_f32_32x32x16_bf16 v[32:47], v[64:67], v[96:99], v[32:47]
	v_max_f32_e32 v64, v128, v129
	v_max3_f32 v64, v64, v130, v131
	v_max3_f32 v64, v64, v132, v133
	v_max3_f32 v64, v64, v134, v135
	v_max3_f32 v64, v64, v136, v137
	v_mfma_f32_32x32x16_bf16 v[32:47], v[68:71], v[108:111], v[32:47]
	v_max3_f32 v64, v64, v138, v139
	v_max3_f32 v66, v64, v140, v141
	ds_read_b64_tr_b16 v[64:65], v182 offset:0x200
	v_max3_f32 v180, v66, v142, v143
	ds_read_b64_tr_b16 v[66:67], v182 offset:0x300
	ds_read_b64_tr_b16 v[68:69], v182 offset:0x1200
	ds_read_b64_tr_b16 v[70:71], v182 offset:0x1300
	v_mfma_f32_32x32x16_bf16 v[32:47], v[72:75], v[100:103], v[32:47]
	ds_read_b64_tr_b16 v[72:73], v182 offset:0x2200
	ds_read_b64_tr_b16 v[74:75], v182 offset:0x2300
	ds_read_b64_tr_b16 v[214:215], v182 offset:0x3200
	ds_read_b64_tr_b16 v[216:217], v182 offset:0x3300
	s_waitcnt lgkmcnt(0)
	v_mfma_f32_32x32x16_bf16 v[32:47], v[76:79], v[104:107], v[32:47]
	v_mfma_f32_32x32x16_bf16 v[48:63], v[64:67], v[96:99], v[48:63]
	v_max3_f32 v76, v180, v112, v113
	v_max3_f32 v64, v76, v114, v115
	ds_read_b64_tr_b16 v[66:67], v182 offset:0x400
	v_max3_f32 v64, v64, v116, v117
	v_max3_f32 v64, v64, v118, v119
	v_max3_f32 v64, v64, v120, v121
	v_max3_f32 v64, v64, v122, v123
	v_mfma_f32_32x32x16_bf16 v[48:63], v[68:71], v[108:111], v[48:63]
	ds_read_b64_tr_b16 v[68:69], v182 offset:0x500
	ds_read_b64_tr_b16 v[70:71], v182 offset:0x1400
	v_max3_f32 v64, v64, v124, v125
	v_max3_f32 v64, v64, v126, v127
	v_mov_b32_e32 v65, v64
	s_nop 1
	v_permlane32_swap_b32_e32 v64, v65
	v_mfma_f32_32x32x16_bf16 v[48:63], v[72:75], v[100:103], v[48:63]
	ds_read_b64_tr_b16 v[72:73], v182 offset:0x1500
	ds_read_b64_tr_b16 v[74:75], v182 offset:0x2400
	ds_read_b64_tr_b16 v[76:77], v182 offset:0x2500
	ds_read_b64_tr_b16 v[218:219], v182 offset:0x3400
	ds_read_b64_tr_b16 v[220:221], v182 offset:0x3500
	s_waitcnt lgkmcnt(0)
	v_mfma_f32_32x32x16_bf16 v[48:63], v[214:217], v[104:107], v[48:63]
	ds_read_b64_tr_b16 v[214:215], v182 offset:0x600
	ds_read_b64_tr_b16 v[216:217], v182 offset:0x700
	ds_read_b64_tr_b16 v[222:223], v182 offset:0x2600
	ds_read_b64_tr_b16 v[224:225], v182 offset:0x2700
	ds_read_b64_tr_b16 v[226:227], v182 offset:0x3600
	ds_read_b64_tr_b16 v[228:229], v182 offset:0x3700
	v_max_f32_e32 v64, v64, v65
	v_mfma_f32_32x32x16_bf16 v[16:31], v[66:69], v[96:99], v[16:31]
	v_cmp_ge_f32_e32 vcc, s15, v64
	s_cmp_eq_u64 vcc, exec
	v_mfma_f32_32x32x16_bf16 v[16:31], v[70:73], v[108:111], v[16:31]
	v_mfma_f32_32x32x16_bf16 v[16:31], v[74:77], v[100:103], v[16:31]
	v_mfma_f32_32x32x16_bf16 v[16:31], v[218:221], v[104:107], v[16:31]
	s_cbranch_scc0 .LBB4_884
	v_mov_b32_e32 v180, 1.0
.LBB4_853:
	ds_read_b64_tr_b16 v[218:219], v182 offset:0x1600
	ds_read_b64_tr_b16 v[220:221], v182 offset:0x1700
	s_waitcnt lgkmcnt(0)
	v_mfma_f32_32x32x16_bf16 v[0:15], v[214:217], v[96:99], v[0:15]
	s_lshl_b32 s2, s57, 14
	s_add_i32 s2, s2, 0
	s_lshl_b32 s3, s57, 13
	v_add_u32_e32 v96, s2, v199
	s_sub_i32 s76, s2, s3
	s_waitcnt vmcnt(0)
	v_add_u32_e32 v97, s2, v200
	v_mfma_f32_32x32x16_bf16 v[0:15], v[218:221], v[108:111], v[0:15]
	ds_write_b128 v96, v[176:179]
	v_add_u32_e32 v96, s76, v201
	ds_write_b128 v97, v[172:175]
	ds_write_b128 v96, v[168:171] offset:49152
	s_andn2_b64 s[2:3], exec, s[30:31]
	s_andn2_b64 vcc, exec, s[30:31]
	v_mfma_f32_32x32x16_bf16 v[0:15], v[222:225], v[100:103], v[0:15]
	v_mfma_f32_32x32x16_bf16 v[0:15], v[226:229], v[104:107], v[0:15]
	s_cbranch_vccnz .LBB4_858
	v_med3_f32 v97, v160, -v255, v255
	v_med3_f32 v98, v164, -v255, v255
	v_cvt_scalef32_pk_fp8_f32 v99, v97, v98, s93
	v_med3_f32 v97, v161, -v255, v255
	v_med3_f32 v98, v165, -v255, v255
	v_cvt_scalef32_pk_fp8_f32 v100, v97, v98, s93
	v_med3_f32 v97, v162, -v255, v255
	v_med3_f32 v98, v166, -v255, v255
	s_bitcmp1_b32 s58, 0
	v_cvt_scalef32_pk_fp8_f32 v101, v97, v98, s93
	s_cselect_b32 s8, 0x1100, 0
	v_med3_f32 v97, v163, -v255, v255
	v_med3_f32 v98, v167, -v255, v255
	v_cmp_eq_u32_e32 vcc, 0, v181
	v_add_u32_e32 v96, s8, v190
	v_cvt_scalef32_pk_fp8_f32 v102, v97, v98, s93
	s_and_b64 vcc, exec, vcc
	s_and_b32 s30, s58, 31
	ds_write_b16 v96, v99
	ds_write_b16 v96, v100 offset:68
	ds_write_b16 v96, v101 offset:136
	ds_write_b16 v96, v102 offset:204
	s_cbranch_vccnz .LBB4_882
	s_lshl_b32 s8, s30, 7
	s_lshl_b32 s9, s58, 6
	s_and_b32 s8, s8, 0xf00
	s_and_b32 s9, s9, 64
	s_or_b32 s26, s8, s9
	s_cbranch_execnz .LBB4_857

; #define AT_SBAR() __builtin_amdgcn_sched_barrier(0)
; template <int D0> DI void pv_one(f32x16& od, int vb, bf16x8 pa0, bf16x8 pa1, bf16x8 pa2, bf16x8 pa3) {
;     const s16x4 l0 = tr_read<v_rd_off(D0, 0, 0)>(vb), h0 = tr_read<v_rd_off(D0, 0, 1)>(vb), l1 = tr_read<v_rd_off(D0, 1, 0)>(vb), h1 = tr_read<v_rd_off(D0, 1, 1)>(vb);
;     const s16x4 l2 = tr_read<v_rd_off(D0, 2, 0)>(vb), h2 = tr_read<v_rd_off(D0, 2, 1)>(vb), l3 = tr_read<v_rd_off(D0, 3, 0)>(vb), h3 = tr_read<v_rd_off(D0, 3, 1)>(vb);
;     asm volatile("s_waitcnt lgkmcnt(0)" ::: "memory"); AT_SBAR();
;     ...
;     od = __builtin_amdgcn_mfma_f32_32x32x16_bf16(AT_PK(l0, h0), pa0, od, 0, 0, 0);
;     od = __builtin_amdgcn_mfma_f32_32x32x16_bf16(AT_PK(l1, h1), pa1, od, 0, 0, 0);
;     od = __builtin_amdgcn_mfma_f32_32x32x16_bf16(AT_PK(l2, h2), pa2, od, 0, 0, 0);
;     od = __builtin_amdgcn_mfma_f32_32x32x16_bf16(AT_PK(l3, h3), pa3, od, 0, 0, 0);
;     ...
; }
; DI void pv_all_sm(f32x16* o, int vb, bf16x8 pa0, bf16x8 pa1, bf16x8 pa2, bf16x8 pa3, f32x16& p0, f32x16& p1, float& m_ref, f32x16& negm, float& alpha) {
;     pv_one<0>(o[0], vb, pa0, pa1, pa2, pa3);
;     float pmax = p0[0];
; #pragma unroll
;     for (int r = 1; r < 16; ++r) pmax = fmaxf(pmax, p0[r]);
;     pv_one<1>(o[1], vb, pa0, pa1, pa2, pa3);
; #pragma unroll
;     for (int r = 0; r < 16; ++r) pmax = fmaxf(pmax, p1[r]);
;     { auto rr = __builtin_amdgcn_permlane32_swap(__float_as_uint(pmax), __float_as_uint(pmax), false, false); pmax = fmaxf(__uint_as_float(rr[0]), __uint_as_float(rr[1])); }
;     pv_one<2>(o[2], vb, pa0, pa1, pa2, pa3);
;     alpha = 1.f;
;     if (__builtin_expect(!__all(pmax <= THRL), 0)) {
;         const float dl = fmaxf(pmax, 0.f); m_ref += dl; alpha = __builtin_amdgcn_exp2f(-dl);
; #pragma unroll
;         for (int r = 0; r < 16; ++r) { p0[r] -= dl; p1[r] -= dl; }
; #pragma unroll
;         for (int r = 0; r < 16; ++r) negm[r] = -m_ref;
;     }
;     pv_one<3>(o[3], vb, pa0, pa1, pa2, pa3);
; #pragma unroll
;     for (int r = 0; r < 16; ++r) p0[r] = __builtin_amdgcn_exp2f(p0[r]);
; }
; DI void attn_pass(const Frame& F, CvRide& cv, const bf16_t* __restrict__ Qb, const bf16_t* __restrict__ Kh, const bf16_t* __restrict__ Vh, char* lds, f32x16 (&o)[4], float& l_out, const int wave_s) {
;     ...
;     const unsigned cv_ldo = (unsigned)(((tid >> 4) * 2 * 2048 + (tid & 15) * 4) * 4), cv_sto = (unsigned)((tid >> 3) * 2048 + 8 * (tid & 7));
.LBB4_872:
	v_lshl_add_u32 v215, s64, 14, v253
	ds_read_b64_tr_b16 v[216:217], v215 offset:0
	ds_read_b64_tr_b16 v[218:219], v215 offset:0x100
	ds_read_b64_tr_b16 v[220:221], v215 offset:0x1000
	ds_read_b64_tr_b16 v[222:223], v215 offset:0x1100
	ds_read_b64_tr_b16 v[224:225], v215 offset:0x2000
	ds_read_b64_tr_b16 v[226:227], v215 offset:0x2100
	ds_read_b64_tr_b16 v[228:229], v215 offset:0x3000
	ds_read_b64_tr_b16 v[230:231], v215 offset:0x3100
	s_waitcnt lgkmcnt(0)
	v_mfma_f32_32x32x16_bf16 v[32:47], v[216:219], v[120:123], v[32:47]
	v_max_f32_e32 v182, v128, v129
	ds_read_b64_tr_b16 v[216:217], v215 offset:0x200
	ds_read_b64_tr_b16 v[218:219], v215 offset:0x300
	v_max3_f32 v182, v182, v130, v131
	v_max3_f32 v182, v182, v132, v133
	v_mfma_f32_32x32x16_bf16 v[32:47], v[220:223], v[124:127], v[32:47]
	ds_read_b64_tr_b16 v[220:221], v215 offset:0x1200
	ds_read_b64_tr_b16 v[222:223], v215 offset:0x1300
	v_max3_f32 v182, v182, v134, v135
	v_max3_f32 v182, v182, v136, v137
	v_max3_f32 v182, v182, v138, v139
	v_max3_f32 v182, v182, v140, v141
	v_max3_f32 v182, v182, v142, v143
	v_mfma_f32_32x32x16_bf16 v[32:47], v[224:227], v[112:115], v[32:47]
	ds_read_b64_tr_b16 v[224:225], v215 offset:0x2200
	ds_read_b64_tr_b16 v[226:227], v215 offset:0x2300
	ds_read_b64_tr_b16 v[232:233], v215 offset:0x3200
	ds_read_b64_tr_b16 v[234:235], v215 offset:0x3300
	s_waitcnt lgkmcnt(0)
	v_mfma_f32_32x32x16_bf16 v[32:47], v[228:231], v[116:119], v[32:47]
	v_mfma_f32_32x32x16_bf16 v[48:63], v[216:219], v[120:123], v[48:63]
	v_max3_f32 v182, v182, v96, v97
	v_max3_f32 v182, v182, v98, v99
	ds_read_b64_tr_b16 v[218:219], v215 offset:0x400
	v_max3_f32 v182, v182, v100, v101
	v_max3_f32 v182, v182, v102, v103
	v_max3_f32 v182, v182, v104, v105
	v_max3_f32 v182, v182, v106, v107
	v_mfma_f32_32x32x16_bf16 v[48:63], v[220:223], v[124:127], v[48:63]
	ds_read_b64_tr_b16 v[220:221], v215 offset:0x500
	ds_read_b64_tr_b16 v[222:223], v215 offset:0x1400
	v_max3_f32 v182, v182, v108, v109
	v_max3_f32 v182, v182, v110, v111
	v_mov_b32_e32 v216, v182
	s_nop 1
	v_permlane32_swap_b32_e32 v182, v216
	v_mfma_f32_32x32x16_bf16 v[48:63], v[224:227], v[112:115], v[48:63]
	ds_read_b64_tr_b16 v[224:225], v215 offset:0x1500
	ds_read_b64_tr_b16 v[226:227], v215 offset:0x2400
	ds_read_b64_tr_b16 v[228:229], v215 offset:0x2500
	ds_read_b64_tr_b16 v[236:237], v215 offset:0x3400
	ds_read_b64_tr_b16 v[238:239], v215 offset:0x3500
	s_waitcnt lgkmcnt(0)
	v_mfma_f32_32x32x16_bf16 v[48:63], v[232:235], v[116:119], v[48:63]
	ds_read_b64_tr_b16 v[230:231], v215 offset:0x3700
	v_max_f32_e32 v216, v182, v216
	v_mfma_f32_32x32x16_bf16 v[16:31], v[218:221], v[120:123], v[16:31]
	v_cmp_ge_f32_e32 vcc, s15, v216
	s_cmp_eq_u64 vcc, exec
	v_mov_b32_e32 v182, 1.0
	v_mfma_f32_32x32x16_bf16 v[16:31], v[222:225], v[124:127], v[16:31]
	v_mfma_f32_32x32x16_bf16 v[16:31], v[226:229], v[112:115], v[16:31]
	v_mfma_f32_32x32x16_bf16 v[16:31], v[236:239], v[116:119], v[16:31]
	s_cbranch_scc0 .LBB4_885
.LBB4_873:
	ds_read_b64_tr_b16 v[216:217], v215 offset:0x600
	ds_read_b64_tr_b16 v[218:219], v215 offset:0x700
	ds_read_b64_tr_b16 v[220:221], v215 offset:0x1600
	ds_read_b64_tr_b16 v[222:223], v215 offset:0x1700
	ds_read_b64_tr_b16 v[224:225], v215 offset:0x2600
	ds_read_b64_tr_b16 v[226:227], v215 offset:0x2700
	ds_read_b64_tr_b16 v[228:229], v215 offset:0x3600
	s_waitcnt lgkmcnt(0)
	v_mfma_f32_32x32x16_bf16 v[0:15], v[216:219], v[120:123], v[0:15]
	s_add_i32 s2, s65, 0
	v_add_u32_e32 v120, s2, v199
	s_waitcnt vmcnt(0)
	ds_write_b128 v120, v[176:179]
	s_mov_b32 s26, 0
	s_andn2_b64 vcc, exec, s[30:31]
	v_mfma_f32_32x32x16_bf16 v[0:15], v[220:223], v[124:127], v[0:15]
	v_mfma_f32_32x32x16_bf16 v[0:15], v[224:227], v[112:115], v[0:15]
	v_add_u32_e32 v112, s2, v200
	ds_write_b128 v112, v[172:175]
	v_lshl_add_u32 v112, s63, 13, v202
	ds_write_b128 v112, v[168:171] offset:49152
	s_andn2_b64 s[2:3], exec, s[30:31]
	v_mfma_f32_32x32x16_bf16 v[0:15], v[228:231], v[116:119], v[0:15]
	s_cbranch_vccnz .LBB4_878
	v_med3_f32 v113, v160, -v255, v255
	v_med3_f32 v114, v164, -v255, v255
	v_cvt_scalef32_pk_fp8_f32 v115, v113, v114, s93
	v_med3_f32 v113, v161, -v255, v255
	v_med3_f32 v114, v165, -v255, v255
	v_cvt_scalef32_pk_fp8_f32 v116, v113, v114, s93
	v_med3_f32 v113, v162, -v255, v255
	v_med3_f32 v114, v166, -v255, v255
	s_bitcmp1_b32 s58, 0
	v_cvt_scalef32_pk_fp8_f32 v117, v113, v114, s93
	s_cselect_b32 s8, 0x1100, 0
	v_med3_f32 v113, v163, -v255, v255
	v_med3_f32 v114, v167, -v255, v255
	v_cmp_eq_u32_e32 vcc, 0, v181
	v_add_u32_e32 v112, s8, v190
	v_cvt_scalef32_pk_fp8_f32 v118, v113, v114, s93
	s_and_b64 vcc, exec, vcc
	s_and_b32 s34, s58, 31
	ds_write_b16 v112, v115
	ds_write_b16 v112, v116 offset:68
	ds_write_b16 v112, v117 offset:136
	ds_write_b16 v112, v118 offset:204
	s_cbranch_vccnz .LBB4_883
	s_lshl_b32 s8, s34, 7
	s_lshl_b32 s9, s58, 6
	s_and_b32 s8, s8, 0xf00
	s_and_b32 s9, s9, 64
	s_or_b32 s26, s8, s9
	s_cbranch_execnz .LBB4_877

; #define AT_SBAR() __builtin_amdgcn_sched_barrier(0)
; template <int OFF> DI s16x4 tr_read(int vb) { s16x4 r; asm volatile("ds_read_b64_tr_b16 %0, %1 offset:%2" : "=&v"(r) : "v"(vb), "i"(OFF) : "memory"); return r; }
; template <int D0> DI void pv_one(f32x16& od, int vb, bf16x8 pa0, bf16x8 pa1, bf16x8 pa2, bf16x8 pa3) {
;     const s16x4 l0 = tr_read<v_rd_off(D0, 0, 0)>(vb), h0 = tr_read<v_rd_off(D0, 0, 1)>(vb), l1 = tr_read<v_rd_off(D0, 1, 0)>(vb), h1 = tr_read<v_rd_off(D0, 1, 1)>(vb);
;     const s16x4 l2 = tr_read<v_rd_off(D0, 2, 0)>(vb), h2 = tr_read<v_rd_off(D0, 2, 1)>(vb), l3 = tr_read<v_rd_off(D0, 3, 0)>(vb), h3 = tr_read<v_rd_off(D0, 3, 1)>(vb);
;     asm volatile("s_waitcnt lgkmcnt(0)" ::: "memory"); AT_SBAR();
;     ...
;     od = __builtin_amdgcn_mfma_f32_32x32x16_bf16(AT_PK(l0, h0), pa0, od, 0, 0, 0);
;     od = __builtin_amdgcn_mfma_f32_32x32x16_bf16(AT_PK(l1, h1), pa1, od, 0, 0, 0);
;     od = __builtin_amdgcn_mfma_f32_32x32x16_bf16(AT_PK(l2, h2), pa2, od, 0, 0, 0);
;     od = __builtin_amdgcn_mfma_f32_32x32x16_bf16(AT_PK(l3, h3), pa3, od, 0, 0, 0);
; DI void attn_pass(const Frame& F, CvRide& cv, const bf16_t* __restrict__ Qb, const bf16_t* __restrict__ Kh, const bf16_t* __restrict__ Vh, char* lds, f32x16 (&o)[4], float& l_out, const int wave_s) {
;     ...
;     const unsigned cv_ldo = (unsigned)(((tid >> 4) * 2 * 2048 + (tid & 15) * 4) * 4), cv_sto = (unsigned)((tid >> 3) * 2048 + 8 * (tid & 7));
;     const int cv_lw = OFF_CV + (4 * (tid & 15)) * 68 + 2 * (tid >> 4), cv_lr = OFF_CV + (tid >> 3) * 68 + 8 * (tid & 7);
;     f32x4 cvA = f32x4{}, cvB = f32x4{}; unsigned cvr0 = 0, cvr1 = 0;
.LBB4_927:
	ds_read_b64_tr_b16 v[218:219], v182 offset:0x600
	ds_read_b64_tr_b16 v[220:221], v182 offset:0x700
	ds_read_b64_tr_b16 v[222:223], v182 offset:0x1600
	ds_read_b64_tr_b16 v[224:225], v182 offset:0x1700
	s_waitcnt lgkmcnt(0)
	v_mfma_f32_32x32x16_bf16 v[0:15], v[218:221], v[96:99], v[0:15]
	s_lshl_b32 s2, s15, 14
	s_add_i32 s2, s2, 0
	s_lshl_b32 s3, s15, 13
	v_add_u32_e32 v96, s2, v203
	s_sub_i32 s54, s2, s3
	s_waitcnt vmcnt(0)
	v_add_u32_e32 v97, s2, v204
	v_mfma_f32_32x32x16_bf16 v[0:15], v[222:225], v[108:111], v[0:15]
	ds_write_b128 v96, v[176:179]
	v_add_u32_e32 v96, s54, v205
	ds_write_b128 v97, v[172:175]
	ds_write_b128 v96, v[168:171] offset:49152
	s_andn2_b64 s[2:3], exec, s[22:23]
	s_andn2_b64 vcc, exec, s[22:23]
	v_mfma_f32_32x32x16_bf16 v[0:15], v[226:229], v[100:103], v[0:15]
	v_mfma_f32_32x32x16_bf16 v[0:15], v[230:233], v[104:107], v[0:15]
	s_cbranch_vccnz .LBB4_932
	v_med3_f32 v97, v160, -v255, v255
	v_med3_f32 v98, v164, -v255, v255
	v_cvt_scalef32_pk_fp8_f32 v99, v97, v98, s93
	v_med3_f32 v97, v161, -v255, v255
	v_med3_f32 v98, v165, -v255, v255
	v_cvt_scalef32_pk_fp8_f32 v100, v97, v98, s93
	v_med3_f32 v97, v162, -v255, v255
	v_med3_f32 v98, v166, -v255, v255
	s_bitcmp1_b32 s58, 0
	v_cvt_scalef32_pk_fp8_f32 v101, v97, v98, s93
	s_cselect_b32 s8, 0x1100, 0
	v_med3_f32 v97, v163, -v255, v255
	v_med3_f32 v98, v167, -v255, v255
	v_cmp_eq_u32_e32 vcc, 0, v181
	v_add_u32_e32 v96, s8, v195
	v_cvt_scalef32_pk_fp8_f32 v102, v97, v98, s93
	s_and_b64 vcc, exec, vcc
	s_and_b32 s22, s58, 31
	ds_write_b16 v96, v99
	ds_write_b16 v96, v100 offset:68
	ds_write_b16 v96, v101 offset:136
	ds_write_b16 v96, v102 offset:204
	s_cbranch_vccnz .LBB4_956
	s_lshl_b32 s8, s22, 7
	s_lshl_b32 s9, s58, 6
	s_and_b32 s8, s8, 0xf00
	s_and_b32 s9, s9, 64
	s_or_b32 s18, s8, s9
	s_cbranch_execnz .LBB4_931

; #define AT_SBAR() __builtin_amdgcn_sched_barrier(0)
; template <int OFF> DI s16x4 tr_read(int vb) { s16x4 r; asm volatile("ds_read_b64_tr_b16 %0, %1 offset:%2" : "=&v"(r) : "v"(vb), "i"(OFF) : "memory"); return r; }
; template <int D0> DI void pv_one(f32x16& od, int vb, bf16x8 pa0, bf16x8 pa1, bf16x8 pa2, bf16x8 pa3) {
;     const s16x4 l0 = tr_read<v_rd_off(D0, 0, 0)>(vb), h0 = tr_read<v_rd_off(D0, 0, 1)>(vb), l1 = tr_read<v_rd_off(D0, 1, 0)>(vb), h1 = tr_read<v_rd_off(D0, 1, 1)>(vb);
;     const s16x4 l2 = tr_read<v_rd_off(D0, 2, 0)>(vb), h2 = tr_read<v_rd_off(D0, 2, 1)>(vb), l3 = tr_read<v_rd_off(D0, 3, 0)>(vb), h3 = tr_read<v_rd_off(D0, 3, 1)>(vb);
;     asm volatile("s_waitcnt lgkmcnt(0)" ::: "memory"); AT_SBAR();
;     ...
;     od = __builtin_amdgcn_mfma_f32_32x32x16_bf16(AT_PK(l0, h0), pa0, od, 0, 0, 0);
;     od = __builtin_amdgcn_mfma_f32_32x32x16_bf16(AT_PK(l1, h1), pa1, od, 0, 0, 0);
;     od = __builtin_amdgcn_mfma_f32_32x32x16_bf16(AT_PK(l2, h2), pa2, od, 0, 0, 0);
;     od = __builtin_amdgcn_mfma_f32_32x32x16_bf16(AT_PK(l3, h3), pa3, od, 0, 0, 0);
; DI void attn_pass(const Frame& F, CvRide& cv, const bf16_t* __restrict__ Qb, const bf16_t* __restrict__ Kh, const bf16_t* __restrict__ Vh, char* lds, f32x16 (&o)[4], float& l_out, const int wave_s) {
;     ...
;     const unsigned cv_ldo = (unsigned)(((tid >> 4) * 2 * 2048 + (tid & 15) * 4) * 4), cv_sto = (unsigned)((tid >> 3) * 2048 + 8 * (tid & 7));
;     const int cv_lw = OFF_CV + (4 * (tid & 15)) * 68 + 2 * (tid >> 4), cv_lr = OFF_CV + (tid >> 3) * 68 + 8 * (tid & 7);
;     f32x4 cvA = f32x4{}, cvB = f32x4{}; unsigned cvr0 = 0, cvr1 = 0;
.LBB4_947:
	ds_read_b64_tr_b16 v[220:221], v219 offset:0x600
	ds_read_b64_tr_b16 v[222:223], v219 offset:0x700
	ds_read_b64_tr_b16 v[224:225], v219 offset:0x1600
	ds_read_b64_tr_b16 v[226:227], v219 offset:0x1700
	ds_read_b64_tr_b16 v[228:229], v219 offset:0x2600
	ds_read_b64_tr_b16 v[230:231], v219 offset:0x2700
	ds_read_b64_tr_b16 v[232:233], v219 offset:0x3600
	s_waitcnt lgkmcnt(0)
	v_mfma_f32_32x32x16_bf16 v[0:15], v[220:223], v[120:123], v[0:15]
	s_add_i32 s2, s31, 0
	v_add_u32_e32 v120, s2, v203
	s_waitcnt vmcnt(0)
	ds_write_b128 v120, v[176:179]
	s_mov_b32 s18, 0
	s_andn2_b64 vcc, exec, s[22:23]
	v_mfma_f32_32x32x16_bf16 v[0:15], v[224:227], v[124:127], v[0:15]
	v_mfma_f32_32x32x16_bf16 v[0:15], v[228:231], v[112:115], v[0:15]
	v_add_u32_e32 v112, s2, v204
	ds_write_b128 v112, v[172:175]
	v_lshl_add_u32 v112, s29, 13, v206
	ds_write_b128 v112, v[168:171] offset:49152
	s_andn2_b64 s[2:3], exec, s[22:23]
	v_mfma_f32_32x32x16_bf16 v[0:15], v[232:235], v[116:119], v[0:15]
	s_cbranch_vccnz .LBB4_952
	v_med3_f32 v113, v160, -v255, v255
	v_med3_f32 v114, v164, -v255, v255
	v_cvt_scalef32_pk_fp8_f32 v115, v113, v114, s93
	v_med3_f32 v113, v161, -v255, v255
	v_med3_f32 v114, v165, -v255, v255
	v_cvt_scalef32_pk_fp8_f32 v116, v113, v114, s93
	v_med3_f32 v113, v162, -v255, v255
	v_med3_f32 v114, v166, -v255, v255
	s_bitcmp1_b32 s58, 0
	v_cvt_scalef32_pk_fp8_f32 v117, v113, v114, s93
	s_cselect_b32 s8, 0x1100, 0
	v_med3_f32 v113, v163, -v255, v255
	v_med3_f32 v114, v167, -v255, v255
	v_cmp_eq_u32_e32 vcc, 0, v181
	v_add_u32_e32 v112, s8, v195
	v_cvt_scalef32_pk_fp8_f32 v118, v113, v114, s93
	s_and_b64 vcc, exec, vcc
	s_and_b32 s24, s58, 31
	ds_write_b16 v112, v115
	ds_write_b16 v112, v116 offset:68
	ds_write_b16 v112, v117 offset:136
	ds_write_b16 v112, v118 offset:204
	s_cbranch_vccnz .LBB4_957
	s_lshl_b32 s8, s24, 7
	s_lshl_b32 s9, s58, 6
	s_and_b32 s8, s8, 0xf00
	s_and_b32 s9, s9, 64
	s_or_b32 s18, s8, s9
	s_cbranch_execnz .LBB4_951
